# MoE K-loops: half-tile units get the same pipelined/interleaved schedule (blocks 1 and 3 only); first reads ordered by first use
# speedup vs baseline: 1.0301x; 1.0037x over previous
.LBB0_726:
	s_cmp_lg_u64 s[2:3], 0
	s_cbranch_scc1 .Lswp_guE_half
	ds_read_b64_tr_b16 v[162:163], v190 offset:0
	ds_read_b64_tr_b16 v[164:165], v191 offset:0
	ds_read_b64_tr_b16 v[170:171], v192 offset:0
	ds_read_b64_tr_b16 v[172:173], v193 offset:0
	ds_read_b128 v[214:217], v207
	ds_read_b128 v[224:227], v207 offset:2048
	ds_read_b128 v[232:235], v207 offset:4096
	ds_read_b128 v[240:243], v207 offset:6144
	ds_read_b64_tr_b16 v[166:167], v190 offset:8192
	ds_read_b64_tr_b16 v[168:169], v191 offset:8192
	ds_read_b64_tr_b16 v[174:175], v192 offset:8192
	ds_read_b64_tr_b16 v[176:177], v193 offset:8192
	ds_read_b128 v[218:221], v207 offset:1024
	ds_read_b128 v[228:231], v207 offset:3072
	ds_read_b128 v[236:239], v207 offset:5120
	ds_read_b128 v[244:247], v207 offset:7168
	s_add_i32 s38, s4, 2
	s_cmp_eq_u32 s34, 28
	s_cselect_b64 s[4:5], -1, 0
	s_and_b64 s[34:35], s[4:5], exec
	s_cselect_b32 s38, 0, s38
	s_cselect_b32 s34, s23, s37
	s_cselect_b32 s35, s22, s36
	s_cselect_b32 s66, s21, s25
	s_cselect_b32 s67, s20, s24
	s_ashr_i32 s39, s38, 31
	s_lshl_b64 s[40:41], s[38:39], 18
	s_add_u32 s68, s67, s40
	s_addc_u32 s69, s66, s41
	s_add_u32 s40, s35, s40
	s_addc_u32 s41, s34, s41
	s_setprio 1
	s_waitcnt lgkmcnt(11)
	v_mfma_f32_16x16x32_bf16 v[158:161], v[162:165], v[214:217], v[158:161]
	v_mfma_f32_16x16x32_bf16 v[154:157], v[170:173], v[214:217], v[154:157]
	ds_read_b128 v[214:217], v207 offset:16384
	s_waitcnt lgkmcnt(11)
	v_mfma_f32_16x16x32_bf16 v[146:149], v[162:165], v[224:227], v[146:149]
	v_mfma_f32_16x16x32_bf16 v[138:141], v[170:173], v[224:227], v[138:141]
	ds_read_b128 v[224:227], v207 offset:18432
	s_waitcnt lgkmcnt(11)
	v_mfma_f32_16x16x32_bf16 v[130:133], v[162:165], v[232:235], v[130:133]
	v_mfma_f32_16x16x32_bf16 v[122:125], v[170:173], v[232:235], v[122:125]
	ds_read_b128 v[232:235], v207 offset:20480
	s_waitcnt lgkmcnt(11)
	v_mfma_f32_16x16x32_bf16 v[114:117], v[162:165], v[240:243], v[114:117]
	v_mfma_f32_16x16x32_bf16 v[106:109], v[170:173], v[240:243], v[106:109]
	ds_read_b128 v[240:243], v207 offset:22528
	s_waitcnt lgkmcnt(7)
	v_mfma_f32_16x16x32_bf16 v[158:161], v[166:169], v[218:221], v[158:161]
	v_mfma_f32_16x16x32_bf16 v[154:157], v[174:177], v[218:221], v[154:157]
	ds_read_b128 v[218:221], v207 offset:17408
	s_waitcnt lgkmcnt(7)
	v_mfma_f32_16x16x32_bf16 v[146:149], v[166:169], v[228:231], v[146:149]
	v_mfma_f32_16x16x32_bf16 v[138:141], v[174:177], v[228:231], v[138:141]
	ds_read_b128 v[228:231], v207 offset:19456
	s_waitcnt lgkmcnt(7)
	v_mfma_f32_16x16x32_bf16 v[130:133], v[166:169], v[236:239], v[130:133]
	v_mfma_f32_16x16x32_bf16 v[122:125], v[174:177], v[236:239], v[122:125]
	ds_read_b128 v[236:239], v207 offset:21504
	s_waitcnt lgkmcnt(7)
	v_mfma_f32_16x16x32_bf16 v[114:117], v[166:169], v[244:247], v[114:117]
	v_mfma_f32_16x16x32_bf16 v[106:109], v[174:177], v[244:247], v[106:109]
	ds_read_b128 v[244:247], v207 offset:23552
	s_waitcnt lgkmcnt(7)
	v_mfma_f32_16x16x32_bf16 v[94:97], v[162:165], v[214:217], v[94:97]
	v_mfma_f32_16x16x32_bf16 v[86:89], v[170:173], v[214:217], v[86:89]
	ds_read_b128 v[214:217], v207
	s_waitcnt lgkmcnt(7)
	v_mfma_f32_16x16x32_bf16 v[78:81], v[162:165], v[224:227], v[78:81]
	v_mfma_f32_16x16x32_bf16 v[70:73], v[170:173], v[224:227], v[70:73]
	ds_read_b128 v[224:227], v207 offset:2048
	s_waitcnt lgkmcnt(7)
	v_mfma_f32_16x16x32_bf16 v[62:65], v[162:165], v[232:235], v[62:65]
	v_mfma_f32_16x16x32_bf16 v[54:57], v[170:173], v[232:235], v[54:57]
	ds_read_b128 v[232:235], v207 offset:4096
	s_waitcnt lgkmcnt(7)
	v_mfma_f32_16x16x32_bf16 v[46:49], v[162:165], v[240:243], v[46:49]
	v_mfma_f32_16x16x32_bf16 v[38:41], v[170:173], v[240:243], v[38:41]
	ds_read_b128 v[240:243], v207 offset:6144
	ds_read_b64_tr_b16 v[162:163], v190 offset:16384
	ds_read_b64_tr_b16 v[164:165], v191 offset:16384
	ds_read_b64_tr_b16 v[170:171], v192 offset:16384
	ds_read_b64_tr_b16 v[172:173], v193 offset:16384
	s_waitcnt lgkmcnt(11)
	v_mfma_f32_16x16x32_bf16 v[94:97], v[166:169], v[218:221], v[94:97]
	v_mfma_f32_16x16x32_bf16 v[86:89], v[174:177], v[218:221], v[86:89]
	ds_read_b128 v[218:221], v207 offset:1024
	s_waitcnt lgkmcnt(11)
	v_mfma_f32_16x16x32_bf16 v[78:81], v[166:169], v[228:231], v[78:81]
	v_mfma_f32_16x16x32_bf16 v[70:73], v[174:177], v[228:231], v[70:73]
	ds_read_b128 v[228:231], v207 offset:3072
	s_waitcnt lgkmcnt(11)
	v_mfma_f32_16x16x32_bf16 v[62:65], v[166:169], v[236:239], v[62:65]
	v_mfma_f32_16x16x32_bf16 v[54:57], v[174:177], v[236:239], v[54:57]
	ds_read_b128 v[236:239], v207 offset:5120
	s_waitcnt lgkmcnt(11)
	v_mfma_f32_16x16x32_bf16 v[46:49], v[166:169], v[244:247], v[46:49]
	v_mfma_f32_16x16x32_bf16 v[38:41], v[174:177], v[244:247], v[38:41]
	ds_read_b128 v[244:247], v207 offset:7168
	ds_read_b64_tr_b16 v[166:167], v190 offset:24576
	ds_read_b64_tr_b16 v[168:169], v191 offset:24576
	ds_read_b64_tr_b16 v[174:175], v192 offset:24576
	ds_read_b64_tr_b16 v[176:177], v193 offset:24576
	s_waitcnt lgkmcnt(8)
	v_mfma_f32_16x16x32_bf16 v[150:153], v[162:165], v[214:217], v[150:153]
	v_mfma_f32_16x16x32_bf16 v[142:145], v[170:173], v[214:217], v[142:145]
	ds_read_b128 v[214:217], v207 offset:16384
	v_mfma_f32_16x16x32_bf16 v[134:137], v[162:165], v[224:227], v[134:137]
	v_mfma_f32_16x16x32_bf16 v[126:129], v[170:173], v[224:227], v[126:129]
	ds_read_b128 v[224:227], v207 offset:18432
	v_mfma_f32_16x16x32_bf16 v[118:121], v[162:165], v[232:235], v[118:121]
	v_mfma_f32_16x16x32_bf16 v[110:113], v[170:173], v[232:235], v[110:113]
	ds_read_b128 v[232:235], v207 offset:20480
	v_mfma_f32_16x16x32_bf16 v[102:105], v[162:165], v[240:243], v[102:105]
	v_mfma_f32_16x16x32_bf16 v[98:101], v[170:173], v[240:243], v[98:101]
	ds_read_b128 v[240:243], v207 offset:22528
	s_waitcnt lgkmcnt(4)
	v_mfma_f32_16x16x32_bf16 v[150:153], v[166:169], v[218:221], v[150:153]
	v_mfma_f32_16x16x32_bf16 v[142:145], v[174:177], v[218:221], v[142:145]
	ds_read_b128 v[218:221], v207 offset:17408
	v_mfma_f32_16x16x32_bf16 v[134:137], v[166:169], v[228:231], v[134:137]
	v_mfma_f32_16x16x32_bf16 v[126:129], v[174:177], v[228:231], v[126:129]
	ds_read_b128 v[228:231], v207 offset:19456
	v_mfma_f32_16x16x32_bf16 v[118:121], v[166:169], v[236:239], v[118:121]
	v_mfma_f32_16x16x32_bf16 v[110:113], v[174:177], v[236:239], v[110:113]
	ds_read_b128 v[236:239], v207 offset:21504
	v_mfma_f32_16x16x32_bf16 v[102:105], v[166:169], v[244:247], v[102:105]
	v_mfma_f32_16x16x32_bf16 v[98:101], v[174:177], v[244:247], v[98:101]
	ds_read_b128 v[244:247], v207 offset:23552
	s_waitcnt lgkmcnt(7)
	v_mfma_f32_16x16x32_bf16 v[90:93], v[162:165], v[214:217], v[90:93]
	v_mfma_f32_16x16x32_bf16 v[82:85], v[170:173], v[214:217], v[82:85]
	s_waitcnt vmcnt(11)
	v_cvt_pk_bf16_f32 v248, v2, v3
	v_cvt_pk_bf16_f32 v249, v4, v5
	ds_write_b64 v199, v[248:249]
	s_add_u32 s70, s40, 0x6000
	s_addc_u32 s71, s41, 0
	global_load_dwordx4 v[2:5], v189, s[70:71]
	s_waitcnt lgkmcnt(7)
	v_mfma_f32_16x16x32_bf16 v[74:77], v[162:165], v[224:227], v[74:77]
	v_mfma_f32_16x16x32_bf16 v[66:69], v[170:173], v[224:227], v[66:69]
	s_waitcnt vmcnt(11)
	v_cvt_pk_bf16_f32 v248, v6, v7
	v_cvt_pk_bf16_f32 v249, v8, v9
	ds_write_b64 v200, v[248:249]
	s_add_u32 s72, s40, 0x4000
	s_addc_u32 s73, s41, 0
	global_load_dwordx4 v[6:9], v189, s[72:73]
	s_waitcnt lgkmcnt(7)
	v_mfma_f32_16x16x32_bf16 v[58:61], v[162:165], v[232:235], v[58:61]
	v_mfma_f32_16x16x32_bf16 v[50:53], v[170:173], v[232:235], v[50:53]
	s_waitcnt vmcnt(11)
	v_cvt_pk_bf16_f32 v248, v10, v11
	v_cvt_pk_bf16_f32 v249, v12, v13
	ds_write_b64 v201, v[248:249]
	s_add_u32 s70, s68, 0x6000
	s_addc_u32 s71, s69, 0
	global_load_dwordx4 v[10:13], v189, s[70:71]
	s_waitcnt lgkmcnt(7)
	v_mfma_f32_16x16x32_bf16 v[42:45], v[162:165], v[240:243], v[42:45]
	v_mfma_f32_16x16x32_bf16 v[30:33], v[170:173], v[240:243], v[30:33]
	s_waitcnt vmcnt(11)
	v_cvt_pk_bf16_f32 v248, v14, v15
	v_cvt_pk_bf16_f32 v249, v16, v17
	ds_write_b64 v202, v[248:249]
	s_add_u32 s72, s40, 0x2000
	s_addc_u32 s73, s41, 0
	global_load_dwordx4 v[14:17], v189, s[72:73]
	s_waitcnt lgkmcnt(7)
	v_mfma_f32_16x16x32_bf16 v[90:93], v[166:169], v[218:221], v[90:93]
	v_mfma_f32_16x16x32_bf16 v[82:85], v[174:177], v[218:221], v[82:85]
	s_waitcnt vmcnt(11)
	v_cvt_pk_bf16_f32 v248, v18, v19
	v_cvt_pk_bf16_f32 v249, v20, v21
	ds_write_b64 v203, v[248:249]
	s_add_u32 s70, s68, 0x4000
	s_addc_u32 s71, s69, 0
	global_load_dwordx4 v[18:21], v189, s[70:71]
	s_waitcnt lgkmcnt(7)
	v_mfma_f32_16x16x32_bf16 v[74:77], v[166:169], v[228:231], v[74:77]
	v_mfma_f32_16x16x32_bf16 v[66:69], v[174:177], v[228:231], v[66:69]
	s_waitcnt vmcnt(11)
	v_cvt_pk_bf16_f32 v248, v22, v23
	v_cvt_pk_bf16_f32 v249, v24, v25
	ds_write_b64 v204, v[248:249]
	global_load_dwordx4 v[22:25], v189, s[40:41]
	s_waitcnt lgkmcnt(7)
	v_mfma_f32_16x16x32_bf16 v[58:61], v[166:169], v[236:239], v[58:61]
	v_mfma_f32_16x16x32_bf16 v[50:53], v[174:177], v[236:239], v[50:53]
	s_waitcnt vmcnt(11)
	v_cvt_pk_bf16_f32 v248, v26, v27
	v_cvt_pk_bf16_f32 v249, v28, v29
	ds_write_b64 v205, v[248:249]
	s_add_u32 s70, s68, 0x2000
	s_addc_u32 s71, s69, 0
	global_load_dwordx4 v[26:29], v189, s[70:71]
	s_waitcnt lgkmcnt(7)
	v_mfma_f32_16x16x32_bf16 v[42:45], v[166:169], v[244:247], v[42:45]
	v_mfma_f32_16x16x32_bf16 v[30:33], v[174:177], v[244:247], v[30:33]
	s_waitcnt vmcnt(11)
	v_cvt_pk_bf16_f32 v248, v34, v35
	v_cvt_pk_bf16_f32 v249, v36, v37
	ds_write_b64 v206, v[248:249]
	global_load_dwordx4 v[34:37], v189, s[68:69]
	s_setprio 0

.LBB0_732:
	s_cmp_lg_u64 s[2:3], 0
	s_cbranch_scc1 .Lswp_guO_half
	ds_read_b64_tr_b16 v[162:163], v190 offset:32768
	ds_read_b64_tr_b16 v[164:165], v191 offset:32768
	ds_read_b64_tr_b16 v[170:171], v192 offset:32768
	ds_read_b64_tr_b16 v[172:173], v193 offset:32768
	ds_read_b128 v[214:217], v207 offset:32768
	ds_read_b128 v[224:227], v207 offset:34816
	ds_read_b128 v[232:235], v207 offset:36864
	ds_read_b128 v[240:243], v207 offset:38912
	ds_read_b64_tr_b16 v[166:167], v190 offset:40960
	ds_read_b64_tr_b16 v[168:169], v191 offset:40960
	ds_read_b64_tr_b16 v[174:175], v192 offset:40960
	ds_read_b64_tr_b16 v[176:177], v193 offset:40960
	ds_read_b128 v[218:221], v207 offset:33792
	ds_read_b128 v[228:231], v207 offset:35840
	ds_read_b128 v[236:239], v207 offset:37888
	ds_read_b128 v[244:247], v207 offset:39936
	s_lshl_b64 s[2:3], s[38:39], 18
	s_add_u32 s4, s2, 0x40000
	s_addc_u32 s5, s3, 0
	s_add_u32 s2, s67, s4
	s_addc_u32 s3, s66, s5
	s_add_u32 s4, s35, s4
	s_addc_u32 s5, s34, s5
	s_setprio 1
	s_waitcnt lgkmcnt(11)
	v_mfma_f32_16x16x32_bf16 v[158:161], v[162:165], v[214:217], v[158:161]
	v_mfma_f32_16x16x32_bf16 v[154:157], v[170:173], v[214:217], v[154:157]
	ds_read_b128 v[214:217], v207 offset:49152
	s_waitcnt lgkmcnt(11)
	v_mfma_f32_16x16x32_bf16 v[146:149], v[162:165], v[224:227], v[146:149]
	v_mfma_f32_16x16x32_bf16 v[138:141], v[170:173], v[224:227], v[138:141]
	ds_read_b128 v[224:227], v207 offset:51200
	s_waitcnt lgkmcnt(11)
	v_mfma_f32_16x16x32_bf16 v[130:133], v[162:165], v[232:235], v[130:133]
	v_mfma_f32_16x16x32_bf16 v[122:125], v[170:173], v[232:235], v[122:125]
	ds_read_b128 v[232:235], v207 offset:53248
	s_waitcnt lgkmcnt(11)
	v_mfma_f32_16x16x32_bf16 v[114:117], v[162:165], v[240:243], v[114:117]
	v_mfma_f32_16x16x32_bf16 v[106:109], v[170:173], v[240:243], v[106:109]
	ds_read_b128 v[240:243], v207 offset:55296
	s_waitcnt lgkmcnt(7)
	v_mfma_f32_16x16x32_bf16 v[158:161], v[166:169], v[218:221], v[158:161]
	v_mfma_f32_16x16x32_bf16 v[154:157], v[174:177], v[218:221], v[154:157]
	ds_read_b128 v[218:221], v207 offset:50176
	s_waitcnt lgkmcnt(7)
	v_mfma_f32_16x16x32_bf16 v[146:149], v[166:169], v[228:231], v[146:149]
	v_mfma_f32_16x16x32_bf16 v[138:141], v[174:177], v[228:231], v[138:141]
	ds_read_b128 v[228:231], v207 offset:52224
	s_waitcnt lgkmcnt(7)
	v_mfma_f32_16x16x32_bf16 v[130:133], v[166:169], v[236:239], v[130:133]
	v_mfma_f32_16x16x32_bf16 v[122:125], v[174:177], v[236:239], v[122:125]
	ds_read_b128 v[236:239], v207 offset:54272
	s_waitcnt lgkmcnt(7)
	v_mfma_f32_16x16x32_bf16 v[114:117], v[166:169], v[244:247], v[114:117]
	v_mfma_f32_16x16x32_bf16 v[106:109], v[174:177], v[244:247], v[106:109]
	ds_read_b128 v[244:247], v207 offset:56320
	s_waitcnt lgkmcnt(7)
	v_mfma_f32_16x16x32_bf16 v[94:97], v[162:165], v[214:217], v[94:97]
	v_mfma_f32_16x16x32_bf16 v[86:89], v[170:173], v[214:217], v[86:89]
	ds_read_b128 v[214:217], v207 offset:32768
	s_waitcnt lgkmcnt(7)
	v_mfma_f32_16x16x32_bf16 v[78:81], v[162:165], v[224:227], v[78:81]
	v_mfma_f32_16x16x32_bf16 v[70:73], v[170:173], v[224:227], v[70:73]
	ds_read_b128 v[224:227], v207 offset:34816
	s_waitcnt lgkmcnt(7)
	v_mfma_f32_16x16x32_bf16 v[62:65], v[162:165], v[232:235], v[62:65]
	v_mfma_f32_16x16x32_bf16 v[54:57], v[170:173], v[232:235], v[54:57]
	ds_read_b128 v[232:235], v207 offset:36864
	s_waitcnt lgkmcnt(7)
	v_mfma_f32_16x16x32_bf16 v[46:49], v[162:165], v[240:243], v[46:49]
	v_mfma_f32_16x16x32_bf16 v[38:41], v[170:173], v[240:243], v[38:41]
	ds_read_b128 v[240:243], v207 offset:38912
	ds_read_b64_tr_b16 v[162:163], v190 offset:49152
	ds_read_b64_tr_b16 v[164:165], v191 offset:49152
	ds_read_b64_tr_b16 v[170:171], v192 offset:49152
	ds_read_b64_tr_b16 v[172:173], v193 offset:49152
	s_waitcnt lgkmcnt(11)
	v_mfma_f32_16x16x32_bf16 v[94:97], v[166:169], v[218:221], v[94:97]
	v_mfma_f32_16x16x32_bf16 v[86:89], v[174:177], v[218:221], v[86:89]
	ds_read_b128 v[218:221], v207 offset:33792
	s_waitcnt lgkmcnt(11)
	v_mfma_f32_16x16x32_bf16 v[78:81], v[166:169], v[228:231], v[78:81]
	v_mfma_f32_16x16x32_bf16 v[70:73], v[174:177], v[228:231], v[70:73]
	ds_read_b128 v[228:231], v207 offset:35840
	s_waitcnt lgkmcnt(11)
	v_mfma_f32_16x16x32_bf16 v[62:65], v[166:169], v[236:239], v[62:65]
	v_mfma_f32_16x16x32_bf16 v[54:57], v[174:177], v[236:239], v[54:57]
	ds_read_b128 v[236:239], v207 offset:37888
	s_waitcnt lgkmcnt(11)
	v_mfma_f32_16x16x32_bf16 v[46:49], v[166:169], v[244:247], v[46:49]
	v_mfma_f32_16x16x32_bf16 v[38:41], v[174:177], v[244:247], v[38:41]
	ds_read_b128 v[244:247], v207 offset:39936
	ds_read_b64_tr_b16 v[166:167], v190 offset:57344
	ds_read_b64_tr_b16 v[168:169], v191 offset:57344
	ds_read_b64_tr_b16 v[174:175], v192 offset:57344
	ds_read_b64_tr_b16 v[176:177], v193 offset:57344
	s_waitcnt lgkmcnt(8)
	v_mfma_f32_16x16x32_bf16 v[150:153], v[162:165], v[214:217], v[150:153]
	v_mfma_f32_16x16x32_bf16 v[142:145], v[170:173], v[214:217], v[142:145]
	ds_read_b128 v[214:217], v207 offset:49152
	v_mfma_f32_16x16x32_bf16 v[134:137], v[162:165], v[224:227], v[134:137]
	v_mfma_f32_16x16x32_bf16 v[126:129], v[170:173], v[224:227], v[126:129]
	ds_read_b128 v[224:227], v207 offset:51200
	v_mfma_f32_16x16x32_bf16 v[118:121], v[162:165], v[232:235], v[118:121]
	v_mfma_f32_16x16x32_bf16 v[110:113], v[170:173], v[232:235], v[110:113]
	ds_read_b128 v[232:235], v207 offset:53248
	v_mfma_f32_16x16x32_bf16 v[102:105], v[162:165], v[240:243], v[102:105]
	v_mfma_f32_16x16x32_bf16 v[98:101], v[170:173], v[240:243], v[98:101]
	ds_read_b128 v[240:243], v207 offset:55296
	s_waitcnt lgkmcnt(4)
	v_mfma_f32_16x16x32_bf16 v[150:153], v[166:169], v[218:221], v[150:153]
	v_mfma_f32_16x16x32_bf16 v[142:145], v[174:177], v[218:221], v[142:145]
	ds_read_b128 v[218:221], v207 offset:50176
	v_mfma_f32_16x16x32_bf16 v[134:137], v[166:169], v[228:231], v[134:137]
	v_mfma_f32_16x16x32_bf16 v[126:129], v[174:177], v[228:231], v[126:129]
	ds_read_b128 v[228:231], v207 offset:52224
	v_mfma_f32_16x16x32_bf16 v[118:121], v[166:169], v[236:239], v[118:121]
	v_mfma_f32_16x16x32_bf16 v[110:113], v[174:177], v[236:239], v[110:113]
	ds_read_b128 v[236:239], v207 offset:54272
	v_mfma_f32_16x16x32_bf16 v[102:105], v[166:169], v[244:247], v[102:105]
	v_mfma_f32_16x16x32_bf16 v[98:101], v[174:177], v[244:247], v[98:101]
	ds_read_b128 v[244:247], v207 offset:56320
	s_waitcnt lgkmcnt(7)
	v_mfma_f32_16x16x32_bf16 v[90:93], v[162:165], v[214:217], v[90:93]
	v_mfma_f32_16x16x32_bf16 v[82:85], v[170:173], v[214:217], v[82:85]
	s_waitcnt vmcnt(9)
	v_cvt_pk_bf16_f32 v248, v2, v3
	v_cvt_pk_bf16_f32 v249, v4, v5
	ds_write_b64 v197, v[248:249] offset:16384
	global_load_dwordx4 v[2:5], v189, s[2:3]
	s_waitcnt lgkmcnt(7)
	v_mfma_f32_16x16x32_bf16 v[74:77], v[162:165], v[224:227], v[74:77]
	v_mfma_f32_16x16x32_bf16 v[66:69], v[170:173], v[224:227], v[66:69]
	s_waitcnt vmcnt(9)
	v_cvt_pk_bf16_f32 v248, v6, v7
	v_cvt_pk_bf16_f32 v249, v8, v9
	ds_write_b64 v196, v[248:249] offset:16384
	global_load_dwordx4 v[6:9], v189, s[4:5]
	s_waitcnt lgkmcnt(7)
	v_mfma_f32_16x16x32_bf16 v[58:61], v[162:165], v[232:235], v[58:61]
	v_mfma_f32_16x16x32_bf16 v[50:53], v[170:173], v[232:235], v[50:53]
	s_waitcnt vmcnt(9)
	v_cvt_pk_bf16_f32 v248, v10, v11
	v_cvt_pk_bf16_f32 v249, v12, v13
	ds_write_b64 v197, v[248:249]
	s_add_u32 s98, s2, 0x2000
	s_addc_u32 s99, s3, 0
	global_load_dwordx4 v[10:13], v189, s[98:99]
	s_waitcnt lgkmcnt(7)
	v_mfma_f32_16x16x32_bf16 v[42:45], v[162:165], v[240:243], v[42:45]
	v_mfma_f32_16x16x32_bf16 v[30:33], v[170:173], v[240:243], v[30:33]
	s_waitcnt vmcnt(9)
	v_cvt_pk_bf16_f32 v248, v14, v15
	v_cvt_pk_bf16_f32 v249, v16, v17
	ds_write_b64 v195, v[248:249] offset:16384
	s_add_u32 s100, s4, 0x2000
	s_addc_u32 s101, s5, 0
	global_load_dwordx4 v[14:17], v189, s[100:101]
	s_waitcnt lgkmcnt(7)
	v_mfma_f32_16x16x32_bf16 v[90:93], v[166:169], v[218:221], v[90:93]
	v_mfma_f32_16x16x32_bf16 v[82:85], v[174:177], v[218:221], v[82:85]
	s_waitcnt vmcnt(9)
	v_cvt_pk_bf16_f32 v248, v18, v19
	v_cvt_pk_bf16_f32 v249, v20, v21
	ds_write_b64 v196, v[248:249]
	s_add_u32 s98, s2, 0x4000
	s_addc_u32 s99, s3, 0
	global_load_dwordx4 v[18:21], v189, s[98:99]
	s_waitcnt lgkmcnt(7)
	v_mfma_f32_16x16x32_bf16 v[74:77], v[166:169], v[228:231], v[74:77]
	v_mfma_f32_16x16x32_bf16 v[66:69], v[174:177], v[228:231], v[66:69]
	s_waitcnt vmcnt(9)
	v_cvt_pk_bf16_f32 v248, v22, v23
	v_cvt_pk_bf16_f32 v249, v24, v25
	ds_write_b64 v194, v[248:249] offset:16384
	s_add_u32 s100, s4, 0x4000
	s_addc_u32 s101, s5, 0
	global_load_dwordx4 v[22:25], v189, s[100:101]
	s_waitcnt lgkmcnt(7)
	v_mfma_f32_16x16x32_bf16 v[58:61], v[166:169], v[236:239], v[58:61]
	v_mfma_f32_16x16x32_bf16 v[50:53], v[174:177], v[236:239], v[50:53]
	s_waitcnt vmcnt(9)
	v_cvt_pk_bf16_f32 v248, v26, v27
	v_cvt_pk_bf16_f32 v249, v28, v29
	ds_write_b64 v195, v[248:249]
	s_add_u32 s98, s2, 0x6000
	s_addc_u32 s99, s3, 0
	global_load_dwordx4 v[26:29], v189, s[98:99]
	s_waitcnt lgkmcnt(7)
	v_mfma_f32_16x16x32_bf16 v[42:45], v[166:169], v[244:247], v[42:45]
	v_mfma_f32_16x16x32_bf16 v[30:33], v[174:177], v[244:247], v[30:33]
	s_waitcnt vmcnt(9)
	v_cvt_pk_bf16_f32 v248, v34, v35
	v_cvt_pk_bf16_f32 v249, v36, v37
	ds_write_b64 v194, v[248:249]
	s_add_u32 s100, s4, 0x6000
	s_addc_u32 s101, s5, 0
	global_load_dwordx4 v[34:37], v189, s[100:101]
	s_setprio 0

.Lswp_guE_half:
	ds_read_b64_tr_b16 v[162:163], v190 offset:0
	ds_read_b64_tr_b16 v[164:165], v191 offset:0
	ds_read_b64_tr_b16 v[170:171], v192 offset:0
	ds_read_b64_tr_b16 v[172:173], v193 offset:0
	ds_read_b128 v[214:217], v207
	ds_read_b128 v[224:227], v207 offset:2048
	ds_read_b128 v[232:235], v207 offset:4096
	ds_read_b128 v[240:243], v207 offset:6144
	ds_read_b64_tr_b16 v[166:167], v190 offset:8192
	ds_read_b64_tr_b16 v[168:169], v191 offset:8192
	ds_read_b64_tr_b16 v[174:175], v192 offset:8192
	ds_read_b64_tr_b16 v[176:177], v193 offset:8192
	ds_read_b128 v[218:221], v207 offset:1024
	ds_read_b128 v[228:231], v207 offset:3072
	ds_read_b128 v[236:239], v207 offset:5120
	ds_read_b128 v[244:247], v207 offset:7168
	s_add_i32 s38, s4, 2
	s_cmp_eq_u32 s34, 28
	s_cselect_b64 s[4:5], -1, 0
	s_and_b64 s[34:35], s[4:5], exec
	s_cselect_b32 s38, 0, s38
	s_cselect_b32 s34, s23, s37
	s_cselect_b32 s35, s22, s36
	s_cselect_b32 s66, s21, s25
	s_cselect_b32 s67, s20, s24
	s_ashr_i32 s39, s38, 31
	s_lshl_b64 s[40:41], s[38:39], 18
	s_add_u32 s68, s67, s40
	s_addc_u32 s69, s66, s41
	s_add_u32 s40, s35, s40
	s_addc_u32 s41, s34, s41
	s_setprio 1
	s_waitcnt lgkmcnt(11)
	v_mfma_f32_16x16x32_bf16 v[158:161], v[162:165], v[214:217], v[158:161]
	v_mfma_f32_16x16x32_bf16 v[154:157], v[170:173], v[214:217], v[154:157]
	ds_read_b128 v[214:217], v207
	s_waitcnt lgkmcnt(11)
	v_mfma_f32_16x16x32_bf16 v[146:149], v[162:165], v[224:227], v[146:149]
	v_mfma_f32_16x16x32_bf16 v[138:141], v[170:173], v[224:227], v[138:141]
	ds_read_b128 v[224:227], v207 offset:2048
	s_waitcnt lgkmcnt(11)
	v_mfma_f32_16x16x32_bf16 v[130:133], v[162:165], v[232:235], v[130:133]
	v_mfma_f32_16x16x32_bf16 v[122:125], v[170:173], v[232:235], v[122:125]
	ds_read_b128 v[232:235], v207 offset:4096
	s_waitcnt lgkmcnt(11)
	v_mfma_f32_16x16x32_bf16 v[114:117], v[162:165], v[240:243], v[114:117]
	v_mfma_f32_16x16x32_bf16 v[106:109], v[170:173], v[240:243], v[106:109]
	ds_read_b128 v[240:243], v207 offset:6144
	ds_read_b64_tr_b16 v[162:163], v190 offset:16384
	ds_read_b64_tr_b16 v[164:165], v191 offset:16384
	ds_read_b64_tr_b16 v[170:171], v192 offset:16384
	ds_read_b64_tr_b16 v[172:173], v193 offset:16384
	s_waitcnt lgkmcnt(11)
	v_mfma_f32_16x16x32_bf16 v[158:161], v[166:169], v[218:221], v[158:161]
	v_mfma_f32_16x16x32_bf16 v[154:157], v[174:177], v[218:221], v[154:157]
	ds_read_b128 v[218:221], v207 offset:1024
	s_waitcnt lgkmcnt(11)
	v_mfma_f32_16x16x32_bf16 v[146:149], v[166:169], v[228:231], v[146:149]
	v_mfma_f32_16x16x32_bf16 v[138:141], v[174:177], v[228:231], v[138:141]
	ds_read_b128 v[228:231], v207 offset:3072
	s_waitcnt lgkmcnt(11)
	v_mfma_f32_16x16x32_bf16 v[130:133], v[166:169], v[236:239], v[130:133]
	v_mfma_f32_16x16x32_bf16 v[122:125], v[174:177], v[236:239], v[122:125]
	ds_read_b128 v[236:239], v207 offset:5120
	s_waitcnt lgkmcnt(11)
	v_mfma_f32_16x16x32_bf16 v[114:117], v[166:169], v[244:247], v[114:117]
	v_mfma_f32_16x16x32_bf16 v[106:109], v[174:177], v[244:247], v[106:109]
	ds_read_b128 v[244:247], v207 offset:7168
	ds_read_b64_tr_b16 v[166:167], v190 offset:24576
	ds_read_b64_tr_b16 v[168:169], v191 offset:24576
	ds_read_b64_tr_b16 v[174:175], v192 offset:24576
	ds_read_b64_tr_b16 v[176:177], v193 offset:24576
	s_waitcnt lgkmcnt(8)
	v_mfma_f32_16x16x32_bf16 v[150:153], v[162:165], v[214:217], v[150:153]
	v_mfma_f32_16x16x32_bf16 v[142:145], v[170:173], v[214:217], v[142:145]
	s_waitcnt vmcnt(9)
	v_cvt_pk_bf16_f32 v248, v2, v3
	v_cvt_pk_bf16_f32 v249, v4, v5
	ds_write_b64 v199, v[248:249]
	s_add_u32 s70, s40, 0x6000
	s_addc_u32 s71, s41, 0
	global_load_dwordx4 v[2:5], v189, s[70:71]
	v_mfma_f32_16x16x32_bf16 v[134:137], v[162:165], v[224:227], v[134:137]
	v_mfma_f32_16x16x32_bf16 v[126:129], v[170:173], v[224:227], v[126:129]
	s_waitcnt vmcnt(9)
	v_cvt_pk_bf16_f32 v248, v6, v7
	v_cvt_pk_bf16_f32 v249, v8, v9
	ds_write_b64 v200, v[248:249]
	s_add_u32 s72, s40, 0x4000
	s_addc_u32 s73, s41, 0
	global_load_dwordx4 v[6:9], v189, s[72:73]
	v_mfma_f32_16x16x32_bf16 v[118:121], v[162:165], v[232:235], v[118:121]
	v_mfma_f32_16x16x32_bf16 v[110:113], v[170:173], v[232:235], v[110:113]
	s_waitcnt vmcnt(9)
	v_cvt_pk_bf16_f32 v248, v10, v11
	v_cvt_pk_bf16_f32 v249, v12, v13
	ds_write_b64 v201, v[248:249]
	s_add_u32 s70, s68, 0x6000
	s_addc_u32 s71, s69, 0
	global_load_dwordx4 v[10:13], v189, s[70:71]
	v_mfma_f32_16x16x32_bf16 v[102:105], v[162:165], v[240:243], v[102:105]
	v_mfma_f32_16x16x32_bf16 v[98:101], v[170:173], v[240:243], v[98:101]
	s_waitcnt vmcnt(9)
	v_cvt_pk_bf16_f32 v248, v14, v15
	v_cvt_pk_bf16_f32 v249, v16, v17
	ds_write_b64 v202, v[248:249]
	s_add_u32 s72, s40, 0x2000
	s_addc_u32 s73, s41, 0
	global_load_dwordx4 v[14:17], v189, s[72:73]
	s_waitcnt lgkmcnt(4)
	v_mfma_f32_16x16x32_bf16 v[150:153], v[166:169], v[218:221], v[150:153]
	v_mfma_f32_16x16x32_bf16 v[142:145], v[174:177], v[218:221], v[142:145]
	s_waitcnt vmcnt(9)
	v_cvt_pk_bf16_f32 v248, v18, v19
	v_cvt_pk_bf16_f32 v249, v20, v21
	ds_write_b64 v203, v[248:249]
	s_add_u32 s70, s68, 0x4000
	s_addc_u32 s71, s69, 0
	global_load_dwordx4 v[18:21], v189, s[70:71]
	v_mfma_f32_16x16x32_bf16 v[134:137], v[166:169], v[228:231], v[134:137]
	v_mfma_f32_16x16x32_bf16 v[126:129], v[174:177], v[228:231], v[126:129]
	s_waitcnt vmcnt(9)
	v_cvt_pk_bf16_f32 v248, v22, v23
	v_cvt_pk_bf16_f32 v249, v24, v25
	ds_write_b64 v204, v[248:249]
	global_load_dwordx4 v[22:25], v189, s[40:41]
	v_mfma_f32_16x16x32_bf16 v[118:121], v[166:169], v[236:239], v[118:121]
	v_mfma_f32_16x16x32_bf16 v[110:113], v[174:177], v[236:239], v[110:113]
	s_waitcnt vmcnt(9)
	v_cvt_pk_bf16_f32 v248, v26, v27
	v_cvt_pk_bf16_f32 v249, v28, v29
	ds_write_b64 v205, v[248:249]
	s_add_u32 s70, s68, 0x2000
	s_addc_u32 s71, s69, 0
	global_load_dwordx4 v[26:29], v189, s[70:71]
	v_mfma_f32_16x16x32_bf16 v[102:105], v[166:169], v[244:247], v[102:105]
	v_mfma_f32_16x16x32_bf16 v[98:101], v[174:177], v[244:247], v[98:101]
	s_waitcnt vmcnt(9)
	v_cvt_pk_bf16_f32 v248, v34, v35
	v_cvt_pk_bf16_f32 v249, v36, v37
	ds_write_b64 v206, v[248:249]
	global_load_dwordx4 v[34:37], v189, s[68:69]
	s_setprio 0
	s_branch .Lswp_guE_tail
.Lswp_guO_half:
	ds_read_b64_tr_b16 v[162:163], v190 offset:32768
	ds_read_b64_tr_b16 v[164:165], v191 offset:32768
	ds_read_b64_tr_b16 v[170:171], v192 offset:32768
	ds_read_b64_tr_b16 v[172:173], v193 offset:32768
	ds_read_b128 v[214:217], v207 offset:32768
	ds_read_b128 v[224:227], v207 offset:34816
	ds_read_b128 v[232:235], v207 offset:36864
	ds_read_b128 v[240:243], v207 offset:38912
	ds_read_b64_tr_b16 v[166:167], v190 offset:40960
	ds_read_b64_tr_b16 v[168:169], v191 offset:40960
	ds_read_b64_tr_b16 v[174:175], v192 offset:40960
	ds_read_b64_tr_b16 v[176:177], v193 offset:40960
	ds_read_b128 v[218:221], v207 offset:33792
	ds_read_b128 v[228:231], v207 offset:35840
	ds_read_b128 v[236:239], v207 offset:37888
	ds_read_b128 v[244:247], v207 offset:39936
	s_lshl_b64 s[2:3], s[38:39], 18
	s_add_u32 s4, s2, 0x40000
	s_addc_u32 s5, s3, 0
	s_add_u32 s2, s67, s4
	s_addc_u32 s3, s66, s5
	s_add_u32 s4, s35, s4
	s_addc_u32 s5, s34, s5
	s_setprio 1
	s_waitcnt lgkmcnt(11)
	v_mfma_f32_16x16x32_bf16 v[158:161], v[162:165], v[214:217], v[158:161]
	v_mfma_f32_16x16x32_bf16 v[154:157], v[170:173], v[214:217], v[154:157]
	ds_read_b128 v[214:217], v207 offset:32768
	s_waitcnt lgkmcnt(11)
	v_mfma_f32_16x16x32_bf16 v[146:149], v[162:165], v[224:227], v[146:149]
	v_mfma_f32_16x16x32_bf16 v[138:141], v[170:173], v[224:227], v[138:141]
	ds_read_b128 v[224:227], v207 offset:34816
	s_waitcnt lgkmcnt(11)
	v_mfma_f32_16x16x32_bf16 v[130:133], v[162:165], v[232:235], v[130:133]
	v_mfma_f32_16x16x32_bf16 v[122:125], v[170:173], v[232:235], v[122:125]
	ds_read_b128 v[232:235], v207 offset:36864
	s_waitcnt lgkmcnt(11)
	v_mfma_f32_16x16x32_bf16 v[114:117], v[162:165], v[240:243], v[114:117]
	v_mfma_f32_16x16x32_bf16 v[106:109], v[170:173], v[240:243], v[106:109]
	ds_read_b128 v[240:243], v207 offset:38912
	ds_read_b64_tr_b16 v[162:163], v190 offset:49152
	ds_read_b64_tr_b16 v[164:165], v191 offset:49152
	ds_read_b64_tr_b16 v[170:171], v192 offset:49152
	ds_read_b64_tr_b16 v[172:173], v193 offset:49152
	s_waitcnt lgkmcnt(11)
	v_mfma_f32_16x16x32_bf16 v[158:161], v[166:169], v[218:221], v[158:161]
	v_mfma_f32_16x16x32_bf16 v[154:157], v[174:177], v[218:221], v[154:157]
	ds_read_b128 v[218:221], v207 offset:33792
	s_waitcnt lgkmcnt(11)
	v_mfma_f32_16x16x32_bf16 v[146:149], v[166:169], v[228:231], v[146:149]
	v_mfma_f32_16x16x32_bf16 v[138:141], v[174:177], v[228:231], v[138:141]
	ds_read_b128 v[228:231], v207 offset:35840
	s_waitcnt lgkmcnt(11)
	v_mfma_f32_16x16x32_bf16 v[130:133], v[166:169], v[236:239], v[130:133]
	v_mfma_f32_16x16x32_bf16 v[122:125], v[174:177], v[236:239], v[122:125]
	ds_read_b128 v[236:239], v207 offset:37888
	s_waitcnt lgkmcnt(11)
	v_mfma_f32_16x16x32_bf16 v[114:117], v[166:169], v[244:247], v[114:117]
	v_mfma_f32_16x16x32_bf16 v[106:109], v[174:177], v[244:247], v[106:109]
	ds_read_b128 v[244:247], v207 offset:39936
	ds_read_b64_tr_b16 v[166:167], v190 offset:57344
	ds_read_b64_tr_b16 v[168:169], v191 offset:57344
	ds_read_b64_tr_b16 v[174:175], v192 offset:57344
	ds_read_b64_tr_b16 v[176:177], v193 offset:57344
	s_waitcnt lgkmcnt(8)
	v_mfma_f32_16x16x32_bf16 v[150:153], v[162:165], v[214:217], v[150:153]
	v_mfma_f32_16x16x32_bf16 v[142:145], v[170:173], v[214:217], v[142:145]
	s_waitcnt vmcnt(9)
	v_cvt_pk_bf16_f32 v248, v2, v3
	v_cvt_pk_bf16_f32 v249, v4, v5
	ds_write_b64 v197, v[248:249] offset:16384
	global_load_dwordx4 v[2:5], v189, s[2:3]
	v_mfma_f32_16x16x32_bf16 v[134:137], v[162:165], v[224:227], v[134:137]
	v_mfma_f32_16x16x32_bf16 v[126:129], v[170:173], v[224:227], v[126:129]
	s_waitcnt vmcnt(9)
	v_cvt_pk_bf16_f32 v248, v6, v7
	v_cvt_pk_bf16_f32 v249, v8, v9
	ds_write_b64 v196, v[248:249] offset:16384
	global_load_dwordx4 v[6:9], v189, s[4:5]
	v_mfma_f32_16x16x32_bf16 v[118:121], v[162:165], v[232:235], v[118:121]
	v_mfma_f32_16x16x32_bf16 v[110:113], v[170:173], v[232:235], v[110:113]
	s_waitcnt vmcnt(9)
	v_cvt_pk_bf16_f32 v248, v10, v11
	v_cvt_pk_bf16_f32 v249, v12, v13
	ds_write_b64 v197, v[248:249]
	s_add_u32 s98, s2, 0x2000
	s_addc_u32 s99, s3, 0
	global_load_dwordx4 v[10:13], v189, s[98:99]
	v_mfma_f32_16x16x32_bf16 v[102:105], v[162:165], v[240:243], v[102:105]
	v_mfma_f32_16x16x32_bf16 v[98:101], v[170:173], v[240:243], v[98:101]
	s_waitcnt vmcnt(9)
	v_cvt_pk_bf16_f32 v248, v14, v15
	v_cvt_pk_bf16_f32 v249, v16, v17
	ds_write_b64 v195, v[248:249] offset:16384
	s_add_u32 s100, s4, 0x2000
	s_addc_u32 s101, s5, 0
	global_load_dwordx4 v[14:17], v189, s[100:101]
	s_waitcnt lgkmcnt(4)
	v_mfma_f32_16x16x32_bf16 v[150:153], v[166:169], v[218:221], v[150:153]
	v_mfma_f32_16x16x32_bf16 v[142:145], v[174:177], v[218:221], v[142:145]
	s_waitcnt vmcnt(9)
	v_cvt_pk_bf16_f32 v248, v18, v19
	v_cvt_pk_bf16_f32 v249, v20, v21
	ds_write_b64 v196, v[248:249]
	s_add_u32 s98, s2, 0x4000
	s_addc_u32 s99, s3, 0
	global_load_dwordx4 v[18:21], v189, s[98:99]
	v_mfma_f32_16x16x32_bf16 v[134:137], v[166:169], v[228:231], v[134:137]
	v_mfma_f32_16x16x32_bf16 v[126:129], v[174:177], v[228:231], v[126:129]
	s_waitcnt vmcnt(9)
	v_cvt_pk_bf16_f32 v248, v22, v23
	v_cvt_pk_bf16_f32 v249, v24, v25
	ds_write_b64 v194, v[248:249] offset:16384
	s_add_u32 s100, s4, 0x4000
	s_addc_u32 s101, s5, 0
	global_load_dwordx4 v[22:25], v189, s[100:101]
	v_mfma_f32_16x16x32_bf16 v[118:121], v[166:169], v[236:239], v[118:121]
	v_mfma_f32_16x16x32_bf16 v[110:113], v[174:177], v[236:239], v[110:113]
	s_waitcnt vmcnt(9)
	v_cvt_pk_bf16_f32 v248, v26, v27
	v_cvt_pk_bf16_f32 v249, v28, v29
	ds_write_b64 v195, v[248:249]
	s_add_u32 s98, s2, 0x6000
	s_addc_u32 s99, s3, 0
	global_load_dwordx4 v[26:29], v189, s[98:99]
	v_mfma_f32_16x16x32_bf16 v[102:105], v[166:169], v[244:247], v[102:105]
	v_mfma_f32_16x16x32_bf16 v[98:101], v[174:177], v[244:247], v[98:101]
	s_waitcnt vmcnt(9)
	v_cvt_pk_bf16_f32 v248, v34, v35
	v_cvt_pk_bf16_f32 v249, v36, v37
	ds_write_b64 v194, v[248:249]
	s_add_u32 s100, s4, 0x6000
	s_addc_u32 s101, s5, 0
	global_load_dwordx4 v[34:37], v189, s[100:101]
	s_setprio 0
	s_branch .Lswp_guO_tail

.LBB0_858:
	s_cmp_lg_u64 s[2:3], 0
	s_cbranch_scc1 .Lswp_dnE_half
	ds_read_b64_tr_b16 v[164:165], v190 offset:0
	ds_read_b64_tr_b16 v[166:167], v191 offset:0
	ds_read_b64_tr_b16 v[172:173], v192 offset:0
	ds_read_b64_tr_b16 v[174:175], v193 offset:0
	ds_read_b128 v[210:213], v207
	ds_read_b128 v[218:221], v207 offset:2048
	ds_read_b128 v[228:231], v207 offset:4096
	ds_read_b128 v[236:239], v207 offset:6144
	ds_read_b64_tr_b16 v[168:169], v190 offset:8192
	ds_read_b64_tr_b16 v[170:171], v191 offset:8192
	ds_read_b64_tr_b16 v[176:177], v192 offset:8192
	ds_read_b64_tr_b16 v[178:179], v193 offset:8192
	ds_read_b128 v[214:217], v207 offset:1024
	ds_read_b128 v[224:227], v207 offset:3072
	ds_read_b128 v[232:235], v207 offset:5120
	ds_read_b128 v[240:243], v207 offset:7168
	s_add_i32 s48, s48, 2
	s_cmp_eq_u32 s35, 12
	s_cselect_b32 s48, 0, s48
	s_cselect_b32 s77, s41, s23
	s_cselect_b32 s82, s40, s22
	s_cselect_b32 s35, s39, s47
	s_cselect_b32 s37, s38, s46
	s_cselect_b32 s43, s27, s45
	s_cselect_b32 s74, s26, s44
	s_cselect_b64 vcc, -1, 0
	s_ashr_i32 s49, s48, 31
	s_lshl_b64 s[50:51], s[48:49], 19
	s_add_u32 s72, s74, s50
	s_addc_u32 s73, s43, s51
	s_add_u32 s50, s37, s50
	s_addc_u32 s51, s35, s51
	s_setprio 1
	s_waitcnt lgkmcnt(11)
	v_mfma_f32_16x16x32_bf16 v[160:163], v[164:167], v[210:213], v[160:163]
	v_mfma_f32_16x16x32_bf16 v[156:159], v[172:175], v[210:213], v[156:159]
	ds_read_b128 v[210:213], v207 offset:16384
	s_waitcnt lgkmcnt(11)
	v_mfma_f32_16x16x32_bf16 v[152:155], v[164:167], v[218:221], v[152:155]
	v_mfma_f32_16x16x32_bf16 v[148:151], v[172:175], v[218:221], v[148:151]
	ds_read_b128 v[218:221], v207 offset:18432
	s_waitcnt lgkmcnt(11)
	v_mfma_f32_16x16x32_bf16 v[136:139], v[164:167], v[228:231], v[136:139]
	v_mfma_f32_16x16x32_bf16 v[132:135], v[172:175], v[228:231], v[132:135]
	ds_read_b128 v[228:231], v207 offset:20480
	s_waitcnt lgkmcnt(11)
	v_mfma_f32_16x16x32_bf16 v[120:123], v[164:167], v[236:239], v[120:123]
	v_mfma_f32_16x16x32_bf16 v[116:119], v[172:175], v[236:239], v[116:119]
	ds_read_b128 v[236:239], v207 offset:22528
	s_waitcnt lgkmcnt(7)
	v_mfma_f32_16x16x32_bf16 v[160:163], v[168:171], v[214:217], v[160:163]
	v_mfma_f32_16x16x32_bf16 v[156:159], v[176:179], v[214:217], v[156:159]
	ds_read_b128 v[214:217], v207 offset:17408
	s_waitcnt lgkmcnt(7)
	v_mfma_f32_16x16x32_bf16 v[152:155], v[168:171], v[224:227], v[152:155]
	v_mfma_f32_16x16x32_bf16 v[148:151], v[176:179], v[224:227], v[148:151]
	ds_read_b128 v[224:227], v207 offset:19456
	s_waitcnt lgkmcnt(7)
	v_mfma_f32_16x16x32_bf16 v[136:139], v[168:171], v[232:235], v[136:139]
	v_mfma_f32_16x16x32_bf16 v[132:135], v[176:179], v[232:235], v[132:135]
	ds_read_b128 v[232:235], v207 offset:21504
	s_waitcnt lgkmcnt(7)
	v_mfma_f32_16x16x32_bf16 v[120:123], v[168:171], v[240:243], v[120:123]
	v_mfma_f32_16x16x32_bf16 v[116:119], v[176:179], v[240:243], v[116:119]
	ds_read_b128 v[240:243], v207 offset:23552
	s_waitcnt lgkmcnt(7)
	v_mfma_f32_16x16x32_bf16 v[80:83], v[164:167], v[210:213], v[80:83]
	v_mfma_f32_16x16x32_bf16 v[68:71], v[172:175], v[210:213], v[68:71]
	ds_read_b128 v[210:213], v207
	s_waitcnt lgkmcnt(7)
	v_mfma_f32_16x16x32_bf16 v[48:51], v[164:167], v[218:221], v[48:51]
	v_mfma_f32_16x16x32_bf16 v[44:47], v[172:175], v[218:221], v[44:47]
	ds_read_b128 v[218:221], v207 offset:2048
	s_waitcnt lgkmcnt(7)
	v_mfma_f32_16x16x32_bf16 v[32:35], v[164:167], v[228:231], v[32:35]
	v_mfma_f32_16x16x32_bf16 v[28:31], v[172:175], v[228:231], v[28:31]
	ds_read_b128 v[228:231], v207 offset:4096
	s_waitcnt lgkmcnt(7)
	v_mfma_f32_16x16x32_bf16 v[16:19], v[164:167], v[236:239], v[16:19]
	v_mfma_f32_16x16x32_bf16 v[12:15], v[172:175], v[236:239], v[12:15]
	ds_read_b128 v[236:239], v207 offset:6144
	ds_read_b64_tr_b16 v[164:165], v190 offset:16384
	ds_read_b64_tr_b16 v[166:167], v191 offset:16384
	ds_read_b64_tr_b16 v[172:173], v192 offset:16384
	ds_read_b64_tr_b16 v[174:175], v193 offset:16384
	s_waitcnt lgkmcnt(11)
	v_mfma_f32_16x16x32_bf16 v[80:83], v[168:171], v[214:217], v[80:83]
	v_mfma_f32_16x16x32_bf16 v[68:71], v[176:179], v[214:217], v[68:71]
	ds_read_b128 v[214:217], v207 offset:1024
	s_waitcnt lgkmcnt(11)
	v_mfma_f32_16x16x32_bf16 v[48:51], v[168:171], v[224:227], v[48:51]
	v_mfma_f32_16x16x32_bf16 v[44:47], v[176:179], v[224:227], v[44:47]
	ds_read_b128 v[224:227], v207 offset:3072
	s_waitcnt lgkmcnt(11)
	v_mfma_f32_16x16x32_bf16 v[32:35], v[168:171], v[232:235], v[32:35]
	v_mfma_f32_16x16x32_bf16 v[28:31], v[176:179], v[232:235], v[28:31]
	ds_read_b128 v[232:235], v207 offset:5120
	s_waitcnt lgkmcnt(11)
	v_mfma_f32_16x16x32_bf16 v[16:19], v[168:171], v[240:243], v[16:19]
	v_mfma_f32_16x16x32_bf16 v[12:15], v[176:179], v[240:243], v[12:15]
	ds_read_b128 v[240:243], v207 offset:7168
	ds_read_b64_tr_b16 v[168:169], v190 offset:24576
	ds_read_b64_tr_b16 v[170:171], v191 offset:24576
	ds_read_b64_tr_b16 v[176:177], v192 offset:24576
	ds_read_b64_tr_b16 v[178:179], v193 offset:24576
	s_waitcnt lgkmcnt(8)
	v_mfma_f32_16x16x32_bf16 v[144:147], v[164:167], v[210:213], v[144:147]
	v_mfma_f32_16x16x32_bf16 v[140:143], v[172:175], v[210:213], v[140:143]
	ds_read_b128 v[210:213], v207 offset:16384
	v_mfma_f32_16x16x32_bf16 v[128:131], v[164:167], v[218:221], v[128:131]
	v_mfma_f32_16x16x32_bf16 v[124:127], v[172:175], v[218:221], v[124:127]
	ds_read_b128 v[218:221], v207 offset:18432
	v_mfma_f32_16x16x32_bf16 v[112:115], v[164:167], v[228:231], v[112:115]
	v_mfma_f32_16x16x32_bf16 v[108:111], v[172:175], v[228:231], v[108:111]
	ds_read_b128 v[228:231], v207 offset:20480
	v_mfma_f32_16x16x32_bf16 v[104:107], v[164:167], v[236:239], v[104:107]
	v_mfma_f32_16x16x32_bf16 v[100:103], v[172:175], v[236:239], v[100:103]
	ds_read_b128 v[236:239], v207 offset:22528
	s_waitcnt lgkmcnt(4)
	v_mfma_f32_16x16x32_bf16 v[144:147], v[168:171], v[214:217], v[144:147]
	v_mfma_f32_16x16x32_bf16 v[140:143], v[176:179], v[214:217], v[140:143]
	ds_read_b128 v[214:217], v207 offset:17408
	v_mfma_f32_16x16x32_bf16 v[128:131], v[168:171], v[224:227], v[128:131]
	v_mfma_f32_16x16x32_bf16 v[124:127], v[176:179], v[224:227], v[124:127]
	ds_read_b128 v[224:227], v207 offset:19456
	v_mfma_f32_16x16x32_bf16 v[112:115], v[168:171], v[232:235], v[112:115]
	v_mfma_f32_16x16x32_bf16 v[108:111], v[176:179], v[232:235], v[108:111]
	ds_read_b128 v[232:235], v207 offset:21504
	v_mfma_f32_16x16x32_bf16 v[104:107], v[168:171], v[240:243], v[104:107]
	v_mfma_f32_16x16x32_bf16 v[100:103], v[176:179], v[240:243], v[100:103]
	ds_read_b128 v[240:243], v207 offset:23552
	s_waitcnt lgkmcnt(7)
	v_mfma_f32_16x16x32_bf16 v[56:59], v[164:167], v[210:213], v[56:59]
	v_mfma_f32_16x16x32_bf16 v[52:55], v[172:175], v[210:213], v[52:55]
	s_waitcnt vmcnt(11)
	v_cvt_pk_bf16_f32 v244, v64, v65
	v_cvt_pk_bf16_f32 v245, v66, v67
	ds_write_b64 v199, v[244:245]
	s_add_u32 s78, s50, 0x8000
	s_addc_u32 s79, s51, 0
	global_load_dwordx4 v[64:67], v189, s[78:79]
	s_waitcnt lgkmcnt(7)
	v_mfma_f32_16x16x32_bf16 v[40:43], v[164:167], v[218:221], v[40:43]
	v_mfma_f32_16x16x32_bf16 v[36:39], v[172:175], v[218:221], v[36:39]
	s_waitcnt vmcnt(11)
	v_cvt_pk_bf16_f32 v244, v60, v61
	v_cvt_pk_bf16_f32 v245, v62, v63
	ds_write_b64 v200, v[244:245]
	s_add_u32 s80, s50, 0xc000
	s_addc_u32 s81, s51, 0
	global_load_dwordx4 v[60:63], v189, s[80:81]
	s_waitcnt lgkmcnt(7)
	v_mfma_f32_16x16x32_bf16 v[24:27], v[164:167], v[228:231], v[24:27]
	v_mfma_f32_16x16x32_bf16 v[20:23], v[172:175], v[228:231], v[20:23]
	s_waitcnt vmcnt(11)
	v_cvt_pk_bf16_f32 v244, v76, v77
	v_cvt_pk_bf16_f32 v245, v78, v79
	ds_write_b64 v201, v[244:245]
	s_add_u32 s78, s50, 0x4000
	s_addc_u32 s79, s51, 0
	global_load_dwordx4 v[76:79], v189, s[78:79]
	s_waitcnt lgkmcnt(7)
	v_mfma_f32_16x16x32_bf16 v[8:11], v[164:167], v[236:239], v[8:11]
	v_mfma_f32_16x16x32_bf16 v[2:5], v[172:175], v[236:239], v[4:7]
	s_waitcnt vmcnt(11)
	v_cvt_pk_bf16_f32 v244, v72, v73
	v_cvt_pk_bf16_f32 v245, v74, v75
	ds_write_b64 v202, v[244:245]
	s_add_u32 s80, s72, 0xc000
	s_addc_u32 s81, s73, 0
	global_load_dwordx4 v[72:75], v189, s[80:81]
	s_waitcnt lgkmcnt(7)
	v_mfma_f32_16x16x32_bf16 v[56:59], v[168:171], v[214:217], v[56:59]
	v_mfma_f32_16x16x32_bf16 v[52:55], v[176:179], v[214:217], v[52:55]
	s_waitcnt vmcnt(11)
	v_cvt_pk_bf16_f32 v244, v88, v89
	v_cvt_pk_bf16_f32 v245, v90, v91
	ds_write_b64 v203, v[244:245]
	global_load_dwordx4 v[88:91], v189, s[50:51]
	s_waitcnt lgkmcnt(7)
	v_mfma_f32_16x16x32_bf16 v[40:43], v[168:171], v[224:227], v[40:43]
	v_mfma_f32_16x16x32_bf16 v[36:39], v[176:179], v[224:227], v[36:39]
	s_waitcnt vmcnt(11)
	v_cvt_pk_bf16_f32 v244, v84, v85
	v_cvt_pk_bf16_f32 v245, v86, v87
	ds_write_b64 v204, v[244:245]
	s_add_u32 s80, s72, 0x8000
	s_addc_u32 s81, s73, 0
	global_load_dwordx4 v[84:87], v189, s[80:81]
	s_waitcnt lgkmcnt(7)
	v_mfma_f32_16x16x32_bf16 v[24:27], v[168:171], v[232:235], v[24:27]
	v_mfma_f32_16x16x32_bf16 v[20:23], v[176:179], v[232:235], v[20:23]
	s_waitcnt vmcnt(11)
	v_cvt_pk_bf16_f32 v244, v96, v97
	v_cvt_pk_bf16_f32 v245, v98, v99
	ds_write_b64 v205, v[244:245]
	global_load_dwordx4 v[96:99], v189, s[72:73]
	s_waitcnt lgkmcnt(7)
	v_mfma_f32_16x16x32_bf16 v[8:11], v[168:171], v[240:243], v[8:11]
	v_mfma_f32_16x16x32_bf16 v[4:7], v[176:179], v[240:243], v[2:5]
	s_waitcnt vmcnt(11)
	v_cvt_pk_bf16_f32 v244, v92, v93
	v_cvt_pk_bf16_f32 v245, v94, v95
	ds_write_b64 v206, v[244:245]
	s_add_u32 s80, s72, 0x4000
	s_addc_u32 s81, s73, 0
	global_load_dwordx4 v[92:95], v189, s[80:81]
	s_setprio 0

.LBB0_864:
	s_cmp_lg_u64 s[2:3], 0
	s_cbranch_scc1 .Lswp_dnO_half
	ds_read_b64_tr_b16 v[164:165], v190 offset:32768
	ds_read_b64_tr_b16 v[166:167], v191 offset:32768
	ds_read_b64_tr_b16 v[172:173], v192 offset:32768
	ds_read_b64_tr_b16 v[174:175], v193 offset:32768
	ds_read_b128 v[210:213], v207 offset:32768
	ds_read_b128 v[218:221], v207 offset:34816
	ds_read_b128 v[228:231], v207 offset:36864
	ds_read_b128 v[236:239], v207 offset:38912
	ds_read_b64_tr_b16 v[168:169], v190 offset:40960
	ds_read_b64_tr_b16 v[170:171], v191 offset:40960
	ds_read_b64_tr_b16 v[176:177], v192 offset:40960
	ds_read_b64_tr_b16 v[178:179], v193 offset:40960
	ds_read_b128 v[214:217], v207 offset:33792
	ds_read_b128 v[224:227], v207 offset:35840
	ds_read_b128 v[232:235], v207 offset:37888
	ds_read_b128 v[240:243], v207 offset:39936
	s_lshl_b64 s[2:3], s[48:49], 19
	s_add_u32 s48, s2, 0x80000
	s_addc_u32 s49, s3, 0
	s_add_u32 s2, s74, s48
	s_addc_u32 s3, s43, s49
	s_add_u32 s48, s37, s48
	s_addc_u32 s49, s35, s49
	s_setprio 1
	s_waitcnt lgkmcnt(11)
	v_mfma_f32_16x16x32_bf16 v[160:163], v[164:167], v[210:213], v[160:163]
	v_mfma_f32_16x16x32_bf16 v[156:159], v[172:175], v[210:213], v[156:159]
	ds_read_b128 v[210:213], v207 offset:49152
	s_waitcnt lgkmcnt(11)
	v_mfma_f32_16x16x32_bf16 v[152:155], v[164:167], v[218:221], v[152:155]
	v_mfma_f32_16x16x32_bf16 v[148:151], v[172:175], v[218:221], v[148:151]
	ds_read_b128 v[218:221], v207 offset:51200
	s_waitcnt lgkmcnt(11)
	v_mfma_f32_16x16x32_bf16 v[136:139], v[164:167], v[228:231], v[136:139]
	v_mfma_f32_16x16x32_bf16 v[132:135], v[172:175], v[228:231], v[132:135]
	ds_read_b128 v[228:231], v207 offset:53248
	s_waitcnt lgkmcnt(11)
	v_mfma_f32_16x16x32_bf16 v[120:123], v[164:167], v[236:239], v[120:123]
	v_mfma_f32_16x16x32_bf16 v[116:119], v[172:175], v[236:239], v[116:119]
	ds_read_b128 v[236:239], v207 offset:55296
	s_waitcnt lgkmcnt(7)
	v_mfma_f32_16x16x32_bf16 v[160:163], v[168:171], v[214:217], v[160:163]
	v_mfma_f32_16x16x32_bf16 v[156:159], v[176:179], v[214:217], v[156:159]
	ds_read_b128 v[214:217], v207 offset:50176
	s_waitcnt lgkmcnt(7)
	v_mfma_f32_16x16x32_bf16 v[152:155], v[168:171], v[224:227], v[152:155]
	v_mfma_f32_16x16x32_bf16 v[148:151], v[176:179], v[224:227], v[148:151]
	ds_read_b128 v[224:227], v207 offset:52224
	s_waitcnt lgkmcnt(7)
	v_mfma_f32_16x16x32_bf16 v[136:139], v[168:171], v[232:235], v[136:139]
	v_mfma_f32_16x16x32_bf16 v[132:135], v[176:179], v[232:235], v[132:135]
	ds_read_b128 v[232:235], v207 offset:54272
	s_waitcnt lgkmcnt(7)
	v_mfma_f32_16x16x32_bf16 v[120:123], v[168:171], v[240:243], v[120:123]
	v_mfma_f32_16x16x32_bf16 v[116:119], v[176:179], v[240:243], v[116:119]
	ds_read_b128 v[240:243], v207 offset:56320
	s_waitcnt lgkmcnt(7)
	v_mfma_f32_16x16x32_bf16 v[80:83], v[164:167], v[210:213], v[80:83]
	v_mfma_f32_16x16x32_bf16 v[68:71], v[172:175], v[210:213], v[68:71]
	ds_read_b128 v[210:213], v207 offset:32768
	s_waitcnt lgkmcnt(7)
	v_mfma_f32_16x16x32_bf16 v[48:51], v[164:167], v[218:221], v[48:51]
	v_mfma_f32_16x16x32_bf16 v[44:47], v[172:175], v[218:221], v[44:47]
	ds_read_b128 v[218:221], v207 offset:34816
	s_waitcnt lgkmcnt(7)
	v_mfma_f32_16x16x32_bf16 v[32:35], v[164:167], v[228:231], v[32:35]
	v_mfma_f32_16x16x32_bf16 v[28:31], v[172:175], v[228:231], v[28:31]
	ds_read_b128 v[228:231], v207 offset:36864
	s_waitcnt lgkmcnt(7)
	v_mfma_f32_16x16x32_bf16 v[16:19], v[164:167], v[236:239], v[16:19]
	v_mfma_f32_16x16x32_bf16 v[12:15], v[172:175], v[236:239], v[12:15]
	ds_read_b128 v[236:239], v207 offset:38912
	ds_read_b64_tr_b16 v[164:165], v190 offset:49152
	ds_read_b64_tr_b16 v[166:167], v191 offset:49152
	ds_read_b64_tr_b16 v[172:173], v192 offset:49152
	ds_read_b64_tr_b16 v[174:175], v193 offset:49152
	s_waitcnt lgkmcnt(11)
	v_mfma_f32_16x16x32_bf16 v[80:83], v[168:171], v[214:217], v[80:83]
	v_mfma_f32_16x16x32_bf16 v[68:71], v[176:179], v[214:217], v[68:71]
	ds_read_b128 v[214:217], v207 offset:33792
	s_waitcnt lgkmcnt(11)
	v_mfma_f32_16x16x32_bf16 v[48:51], v[168:171], v[224:227], v[48:51]
	v_mfma_f32_16x16x32_bf16 v[44:47], v[176:179], v[224:227], v[44:47]
	ds_read_b128 v[224:227], v207 offset:35840
	s_waitcnt lgkmcnt(11)
	v_mfma_f32_16x16x32_bf16 v[32:35], v[168:171], v[232:235], v[32:35]
	v_mfma_f32_16x16x32_bf16 v[28:31], v[176:179], v[232:235], v[28:31]
	ds_read_b128 v[232:235], v207 offset:37888
	s_waitcnt lgkmcnt(11)
	v_mfma_f32_16x16x32_bf16 v[16:19], v[168:171], v[240:243], v[16:19]
	v_mfma_f32_16x16x32_bf16 v[12:15], v[176:179], v[240:243], v[12:15]
	ds_read_b128 v[240:243], v207 offset:39936
	ds_read_b64_tr_b16 v[168:169], v190 offset:57344
	ds_read_b64_tr_b16 v[170:171], v191 offset:57344
	ds_read_b64_tr_b16 v[176:177], v192 offset:57344
	ds_read_b64_tr_b16 v[178:179], v193 offset:57344
	s_waitcnt lgkmcnt(8)
	v_mfma_f32_16x16x32_bf16 v[144:147], v[164:167], v[210:213], v[144:147]
	v_mfma_f32_16x16x32_bf16 v[140:143], v[172:175], v[210:213], v[140:143]
	ds_read_b128 v[210:213], v207 offset:49152
	v_mfma_f32_16x16x32_bf16 v[128:131], v[164:167], v[218:221], v[128:131]
	v_mfma_f32_16x16x32_bf16 v[124:127], v[172:175], v[218:221], v[124:127]
	ds_read_b128 v[218:221], v207 offset:51200
	v_mfma_f32_16x16x32_bf16 v[112:115], v[164:167], v[228:231], v[112:115]
	v_mfma_f32_16x16x32_bf16 v[108:111], v[172:175], v[228:231], v[108:111]
	ds_read_b128 v[228:231], v207 offset:53248
	v_mfma_f32_16x16x32_bf16 v[104:107], v[164:167], v[236:239], v[104:107]
	v_mfma_f32_16x16x32_bf16 v[100:103], v[172:175], v[236:239], v[100:103]
	ds_read_b128 v[236:239], v207 offset:55296
	s_waitcnt lgkmcnt(4)
	v_mfma_f32_16x16x32_bf16 v[144:147], v[168:171], v[214:217], v[144:147]
	v_mfma_f32_16x16x32_bf16 v[140:143], v[176:179], v[214:217], v[140:143]
	ds_read_b128 v[214:217], v207 offset:50176
	v_mfma_f32_16x16x32_bf16 v[128:131], v[168:171], v[224:227], v[128:131]
	v_mfma_f32_16x16x32_bf16 v[124:127], v[176:179], v[224:227], v[124:127]
	ds_read_b128 v[224:227], v207 offset:52224
	v_mfma_f32_16x16x32_bf16 v[112:115], v[168:171], v[232:235], v[112:115]
	v_mfma_f32_16x16x32_bf16 v[108:111], v[176:179], v[232:235], v[108:111]
	ds_read_b128 v[232:235], v207 offset:54272
	v_mfma_f32_16x16x32_bf16 v[104:107], v[168:171], v[240:243], v[104:107]
	v_mfma_f32_16x16x32_bf16 v[100:103], v[176:179], v[240:243], v[100:103]
	ds_read_b128 v[240:243], v207 offset:56320
	s_waitcnt lgkmcnt(7)
	v_mfma_f32_16x16x32_bf16 v[56:59], v[164:167], v[210:213], v[56:59]
	v_mfma_f32_16x16x32_bf16 v[52:55], v[172:175], v[210:213], v[52:55]
	s_waitcnt vmcnt(9)
	v_cvt_pk_bf16_f32 v244, v64, v65
	v_cvt_pk_bf16_f32 v245, v66, v67
	ds_write_b64 v196, v[244:245] offset:16384
	global_load_dwordx4 v[64:67], v189, s[2:3]
	s_waitcnt lgkmcnt(7)
	v_mfma_f32_16x16x32_bf16 v[40:43], v[164:167], v[218:221], v[40:43]
	v_mfma_f32_16x16x32_bf16 v[36:39], v[172:175], v[218:221], v[36:39]
	s_waitcnt vmcnt(9)
	v_cvt_pk_bf16_f32 v244, v60, v61
	v_cvt_pk_bf16_f32 v245, v62, v63
	ds_write_b64 v197, v[244:245] offset:16384
	global_load_dwordx4 v[60:63], v189, s[48:49]
	s_waitcnt lgkmcnt(7)
	v_mfma_f32_16x16x32_bf16 v[24:27], v[164:167], v[228:231], v[24:27]
	v_mfma_f32_16x16x32_bf16 v[20:23], v[172:175], v[228:231], v[20:23]
	s_waitcnt vmcnt(9)
	v_cvt_pk_bf16_f32 v244, v76, v77
	v_cvt_pk_bf16_f32 v245, v78, v79
	ds_write_b64 v195, v[244:245] offset:16384
	s_add_u32 s98, s2, 0x4000
	s_addc_u32 s99, s3, 0
	global_load_dwordx4 v[76:79], v189, s[98:99]
	s_waitcnt lgkmcnt(7)
	v_mfma_f32_16x16x32_bf16 v[8:11], v[164:167], v[236:239], v[8:11]
	v_mfma_f32_16x16x32_bf16 v[2:5], v[172:175], v[236:239], v[4:7]
	s_waitcnt vmcnt(9)
	v_cvt_pk_bf16_f32 v244, v72, v73
	v_cvt_pk_bf16_f32 v245, v74, v75
	ds_write_b64 v197, v[244:245]
	s_add_u32 s100, s48, 0x4000
	s_addc_u32 s101, s49, 0
	global_load_dwordx4 v[72:75], v189, s[100:101]
	s_waitcnt lgkmcnt(7)
	v_mfma_f32_16x16x32_bf16 v[56:59], v[168:171], v[214:217], v[56:59]
	v_mfma_f32_16x16x32_bf16 v[52:55], v[176:179], v[214:217], v[52:55]
	s_waitcnt vmcnt(9)
	v_cvt_pk_bf16_f32 v244, v88, v89
	v_cvt_pk_bf16_f32 v245, v90, v91
	ds_write_b64 v194, v[244:245] offset:16384
	s_add_u32 s98, s2, 0x8000
	s_addc_u32 s99, s3, 0
	global_load_dwordx4 v[88:91], v189, s[98:99]
	s_waitcnt lgkmcnt(7)
	v_mfma_f32_16x16x32_bf16 v[40:43], v[168:171], v[224:227], v[40:43]
	v_mfma_f32_16x16x32_bf16 v[36:39], v[176:179], v[224:227], v[36:39]
	s_waitcnt vmcnt(9)
	v_cvt_pk_bf16_f32 v244, v84, v85
	v_cvt_pk_bf16_f32 v245, v86, v87
	ds_write_b64 v196, v[244:245]
	s_add_u32 s100, s48, 0x8000
	s_addc_u32 s101, s49, 0
	global_load_dwordx4 v[84:87], v189, s[100:101]
	s_waitcnt lgkmcnt(7)
	v_mfma_f32_16x16x32_bf16 v[24:27], v[168:171], v[232:235], v[24:27]
	v_mfma_f32_16x16x32_bf16 v[20:23], v[176:179], v[232:235], v[20:23]
	s_waitcnt vmcnt(9)
	v_cvt_pk_bf16_f32 v244, v96, v97
	v_cvt_pk_bf16_f32 v245, v98, v99
	ds_write_b64 v194, v[244:245]
	s_add_u32 s98, s2, 0xc000
	s_addc_u32 s99, s3, 0
	global_load_dwordx4 v[96:99], v189, s[98:99]
	s_waitcnt lgkmcnt(7)
	v_mfma_f32_16x16x32_bf16 v[8:11], v[168:171], v[240:243], v[8:11]
	v_mfma_f32_16x16x32_bf16 v[4:7], v[176:179], v[240:243], v[2:5]
	s_waitcnt vmcnt(9)
	v_cvt_pk_bf16_f32 v244, v92, v93
	v_cvt_pk_bf16_f32 v245, v94, v95
	ds_write_b64 v195, v[244:245]
	s_add_u32 s100, s48, 0xc000
	s_addc_u32 s101, s49, 0
	global_load_dwordx4 v[92:95], v189, s[100:101]
	s_setprio 0

.Lswp_dnE_half:
	ds_read_b64_tr_b16 v[164:165], v190 offset:0
	ds_read_b64_tr_b16 v[166:167], v191 offset:0
	ds_read_b64_tr_b16 v[172:173], v192 offset:0
	ds_read_b64_tr_b16 v[174:175], v193 offset:0
	ds_read_b128 v[210:213], v207
	ds_read_b128 v[218:221], v207 offset:2048
	ds_read_b128 v[228:231], v207 offset:4096
	ds_read_b128 v[236:239], v207 offset:6144
	ds_read_b64_tr_b16 v[168:169], v190 offset:8192
	ds_read_b64_tr_b16 v[170:171], v191 offset:8192
	ds_read_b64_tr_b16 v[176:177], v192 offset:8192
	ds_read_b64_tr_b16 v[178:179], v193 offset:8192
	ds_read_b128 v[214:217], v207 offset:1024
	ds_read_b128 v[224:227], v207 offset:3072
	ds_read_b128 v[232:235], v207 offset:5120
	ds_read_b128 v[240:243], v207 offset:7168
	s_add_i32 s48, s48, 2
	s_cmp_eq_u32 s35, 12
	s_cselect_b32 s48, 0, s48
	s_cselect_b32 s77, s41, s23
	s_cselect_b32 s82, s40, s22
	s_cselect_b32 s35, s39, s47
	s_cselect_b32 s37, s38, s46
	s_cselect_b32 s43, s27, s45
	s_cselect_b32 s74, s26, s44
	s_cselect_b64 vcc, -1, 0
	s_ashr_i32 s49, s48, 31
	s_lshl_b64 s[50:51], s[48:49], 19
	s_add_u32 s72, s74, s50
	s_addc_u32 s73, s43, s51
	s_add_u32 s50, s37, s50
	s_addc_u32 s51, s35, s51
	s_setprio 1
	s_waitcnt lgkmcnt(11)
	v_mfma_f32_16x16x32_bf16 v[160:163], v[164:167], v[210:213], v[160:163]
	v_mfma_f32_16x16x32_bf16 v[156:159], v[172:175], v[210:213], v[156:159]
	ds_read_b128 v[210:213], v207
	s_waitcnt lgkmcnt(11)
	v_mfma_f32_16x16x32_bf16 v[152:155], v[164:167], v[218:221], v[152:155]
	v_mfma_f32_16x16x32_bf16 v[148:151], v[172:175], v[218:221], v[148:151]
	ds_read_b128 v[218:221], v207 offset:2048
	s_waitcnt lgkmcnt(11)
	v_mfma_f32_16x16x32_bf16 v[136:139], v[164:167], v[228:231], v[136:139]
	v_mfma_f32_16x16x32_bf16 v[132:135], v[172:175], v[228:231], v[132:135]
	ds_read_b128 v[228:231], v207 offset:4096
	s_waitcnt lgkmcnt(11)
	v_mfma_f32_16x16x32_bf16 v[120:123], v[164:167], v[236:239], v[120:123]
	v_mfma_f32_16x16x32_bf16 v[116:119], v[172:175], v[236:239], v[116:119]
	ds_read_b128 v[236:239], v207 offset:6144
	ds_read_b64_tr_b16 v[164:165], v190 offset:16384
	ds_read_b64_tr_b16 v[166:167], v191 offset:16384
	ds_read_b64_tr_b16 v[172:173], v192 offset:16384
	ds_read_b64_tr_b16 v[174:175], v193 offset:16384
	s_waitcnt lgkmcnt(11)
	v_mfma_f32_16x16x32_bf16 v[160:163], v[168:171], v[214:217], v[160:163]
	v_mfma_f32_16x16x32_bf16 v[156:159], v[176:179], v[214:217], v[156:159]
	ds_read_b128 v[214:217], v207 offset:1024
	s_waitcnt lgkmcnt(11)
	v_mfma_f32_16x16x32_bf16 v[152:155], v[168:171], v[224:227], v[152:155]
	v_mfma_f32_16x16x32_bf16 v[148:151], v[176:179], v[224:227], v[148:151]
	ds_read_b128 v[224:227], v207 offset:3072
	s_waitcnt lgkmcnt(11)
	v_mfma_f32_16x16x32_bf16 v[136:139], v[168:171], v[232:235], v[136:139]
	v_mfma_f32_16x16x32_bf16 v[132:135], v[176:179], v[232:235], v[132:135]
	ds_read_b128 v[232:235], v207 offset:5120
	s_waitcnt lgkmcnt(11)
	v_mfma_f32_16x16x32_bf16 v[120:123], v[168:171], v[240:243], v[120:123]
	v_mfma_f32_16x16x32_bf16 v[116:119], v[176:179], v[240:243], v[116:119]
	ds_read_b128 v[240:243], v207 offset:7168
	ds_read_b64_tr_b16 v[168:169], v190 offset:24576
	ds_read_b64_tr_b16 v[170:171], v191 offset:24576
	ds_read_b64_tr_b16 v[176:177], v192 offset:24576
	ds_read_b64_tr_b16 v[178:179], v193 offset:24576
	s_waitcnt lgkmcnt(8)
	v_mfma_f32_16x16x32_bf16 v[144:147], v[164:167], v[210:213], v[144:147]
	v_mfma_f32_16x16x32_bf16 v[140:143], v[172:175], v[210:213], v[140:143]
	s_waitcnt vmcnt(9)
	v_cvt_pk_bf16_f32 v244, v64, v65
	v_cvt_pk_bf16_f32 v245, v66, v67
	ds_write_b64 v199, v[244:245]
	s_add_u32 s78, s50, 0x8000
	s_addc_u32 s79, s51, 0
	global_load_dwordx4 v[64:67], v189, s[78:79]
	v_mfma_f32_16x16x32_bf16 v[128:131], v[164:167], v[218:221], v[128:131]
	v_mfma_f32_16x16x32_bf16 v[124:127], v[172:175], v[218:221], v[124:127]
	s_waitcnt vmcnt(9)
	v_cvt_pk_bf16_f32 v244, v60, v61
	v_cvt_pk_bf16_f32 v245, v62, v63
	ds_write_b64 v200, v[244:245]
	s_add_u32 s80, s50, 0xc000
	s_addc_u32 s81, s51, 0
	global_load_dwordx4 v[60:63], v189, s[80:81]
	v_mfma_f32_16x16x32_bf16 v[112:115], v[164:167], v[228:231], v[112:115]
	v_mfma_f32_16x16x32_bf16 v[108:111], v[172:175], v[228:231], v[108:111]
	s_waitcnt vmcnt(9)
	v_cvt_pk_bf16_f32 v244, v76, v77
	v_cvt_pk_bf16_f32 v245, v78, v79
	ds_write_b64 v201, v[244:245]
	s_add_u32 s78, s50, 0x4000
	s_addc_u32 s79, s51, 0
	global_load_dwordx4 v[76:79], v189, s[78:79]
	v_mfma_f32_16x16x32_bf16 v[104:107], v[164:167], v[236:239], v[104:107]
	v_mfma_f32_16x16x32_bf16 v[100:103], v[172:175], v[236:239], v[100:103]
	s_waitcnt vmcnt(9)
	v_cvt_pk_bf16_f32 v244, v72, v73
	v_cvt_pk_bf16_f32 v245, v74, v75
	ds_write_b64 v202, v[244:245]
	s_add_u32 s80, s72, 0xc000
	s_addc_u32 s81, s73, 0
	global_load_dwordx4 v[72:75], v189, s[80:81]
	s_waitcnt lgkmcnt(4)
	v_mfma_f32_16x16x32_bf16 v[144:147], v[168:171], v[214:217], v[144:147]
	v_mfma_f32_16x16x32_bf16 v[140:143], v[176:179], v[214:217], v[140:143]
	s_waitcnt vmcnt(9)
	v_cvt_pk_bf16_f32 v244, v88, v89
	v_cvt_pk_bf16_f32 v245, v90, v91
	ds_write_b64 v203, v[244:245]
	global_load_dwordx4 v[88:91], v189, s[50:51]
	v_mfma_f32_16x16x32_bf16 v[128:131], v[168:171], v[224:227], v[128:131]
	v_mfma_f32_16x16x32_bf16 v[124:127], v[176:179], v[224:227], v[124:127]
	s_waitcnt vmcnt(9)
	v_cvt_pk_bf16_f32 v244, v84, v85
	v_cvt_pk_bf16_f32 v245, v86, v87
	ds_write_b64 v204, v[244:245]
	s_add_u32 s80, s72, 0x8000
	s_addc_u32 s81, s73, 0
	global_load_dwordx4 v[84:87], v189, s[80:81]
	v_mfma_f32_16x16x32_bf16 v[112:115], v[168:171], v[232:235], v[112:115]
	v_mfma_f32_16x16x32_bf16 v[108:111], v[176:179], v[232:235], v[108:111]
	s_waitcnt vmcnt(9)
	v_cvt_pk_bf16_f32 v244, v96, v97
	v_cvt_pk_bf16_f32 v245, v98, v99
	ds_write_b64 v205, v[244:245]
	global_load_dwordx4 v[96:99], v189, s[72:73]
	v_mfma_f32_16x16x32_bf16 v[104:107], v[168:171], v[240:243], v[104:107]
	v_mfma_f32_16x16x32_bf16 v[100:103], v[176:179], v[240:243], v[100:103]
	s_waitcnt vmcnt(9)
	v_cvt_pk_bf16_f32 v244, v92, v93
	v_cvt_pk_bf16_f32 v245, v94, v95
	ds_write_b64 v206, v[244:245]
	s_add_u32 s80, s72, 0x4000
	s_addc_u32 s81, s73, 0
	global_load_dwordx4 v[92:95], v189, s[80:81]
	s_setprio 0
	s_branch .Lswp_dnE_tail
.Lswp_dnO_half:
	ds_read_b64_tr_b16 v[164:165], v190 offset:32768
	ds_read_b64_tr_b16 v[166:167], v191 offset:32768
	ds_read_b64_tr_b16 v[172:173], v192 offset:32768
	ds_read_b64_tr_b16 v[174:175], v193 offset:32768
	ds_read_b128 v[210:213], v207 offset:32768
	ds_read_b128 v[218:221], v207 offset:34816
	ds_read_b128 v[228:231], v207 offset:36864
	ds_read_b128 v[236:239], v207 offset:38912
	ds_read_b64_tr_b16 v[168:169], v190 offset:40960
	ds_read_b64_tr_b16 v[170:171], v191 offset:40960
	ds_read_b64_tr_b16 v[176:177], v192 offset:40960
	ds_read_b64_tr_b16 v[178:179], v193 offset:40960
	ds_read_b128 v[214:217], v207 offset:33792
	ds_read_b128 v[224:227], v207 offset:35840
	ds_read_b128 v[232:235], v207 offset:37888
	ds_read_b128 v[240:243], v207 offset:39936
	s_lshl_b64 s[2:3], s[48:49], 19
	s_add_u32 s48, s2, 0x80000
	s_addc_u32 s49, s3, 0
	s_add_u32 s2, s74, s48
	s_addc_u32 s3, s43, s49
	s_add_u32 s48, s37, s48
	s_addc_u32 s49, s35, s49
	s_setprio 1
	s_waitcnt lgkmcnt(11)
	v_mfma_f32_16x16x32_bf16 v[160:163], v[164:167], v[210:213], v[160:163]
	v_mfma_f32_16x16x32_bf16 v[156:159], v[172:175], v[210:213], v[156:159]
	ds_read_b128 v[210:213], v207 offset:32768
	s_waitcnt lgkmcnt(11)
	v_mfma_f32_16x16x32_bf16 v[152:155], v[164:167], v[218:221], v[152:155]
	v_mfma_f32_16x16x32_bf16 v[148:151], v[172:175], v[218:221], v[148:151]
	ds_read_b128 v[218:221], v207 offset:34816
	s_waitcnt lgkmcnt(11)
	v_mfma_f32_16x16x32_bf16 v[136:139], v[164:167], v[228:231], v[136:139]
	v_mfma_f32_16x16x32_bf16 v[132:135], v[172:175], v[228:231], v[132:135]
	ds_read_b128 v[228:231], v207 offset:36864
	s_waitcnt lgkmcnt(11)
	v_mfma_f32_16x16x32_bf16 v[120:123], v[164:167], v[236:239], v[120:123]
	v_mfma_f32_16x16x32_bf16 v[116:119], v[172:175], v[236:239], v[116:119]
	ds_read_b128 v[236:239], v207 offset:38912
	ds_read_b64_tr_b16 v[164:165], v190 offset:49152
	ds_read_b64_tr_b16 v[166:167], v191 offset:49152
	ds_read_b64_tr_b16 v[172:173], v192 offset:49152
	ds_read_b64_tr_b16 v[174:175], v193 offset:49152
	s_waitcnt lgkmcnt(11)
	v_mfma_f32_16x16x32_bf16 v[160:163], v[168:171], v[214:217], v[160:163]
	v_mfma_f32_16x16x32_bf16 v[156:159], v[176:179], v[214:217], v[156:159]
	ds_read_b128 v[214:217], v207 offset:33792
	s_waitcnt lgkmcnt(11)
	v_mfma_f32_16x16x32_bf16 v[152:155], v[168:171], v[224:227], v[152:155]
	v_mfma_f32_16x16x32_bf16 v[148:151], v[176:179], v[224:227], v[148:151]
	ds_read_b128 v[224:227], v207 offset:35840
	s_waitcnt lgkmcnt(11)
	v_mfma_f32_16x16x32_bf16 v[136:139], v[168:171], v[232:235], v[136:139]
	v_mfma_f32_16x16x32_bf16 v[132:135], v[176:179], v[232:235], v[132:135]
	ds_read_b128 v[232:235], v207 offset:37888
	s_waitcnt lgkmcnt(11)
	v_mfma_f32_16x16x32_bf16 v[120:123], v[168:171], v[240:243], v[120:123]
	v_mfma_f32_16x16x32_bf16 v[116:119], v[176:179], v[240:243], v[116:119]
	ds_read_b128 v[240:243], v207 offset:39936
	ds_read_b64_tr_b16 v[168:169], v190 offset:57344
	ds_read_b64_tr_b16 v[170:171], v191 offset:57344
	ds_read_b64_tr_b16 v[176:177], v192 offset:57344
	ds_read_b64_tr_b16 v[178:179], v193 offset:57344
	s_waitcnt lgkmcnt(8)
	v_mfma_f32_16x16x32_bf16 v[144:147], v[164:167], v[210:213], v[144:147]
	v_mfma_f32_16x16x32_bf16 v[140:143], v[172:175], v[210:213], v[140:143]
	s_waitcnt vmcnt(9)
	v_cvt_pk_bf16_f32 v244, v64, v65
	v_cvt_pk_bf16_f32 v245, v66, v67
	ds_write_b64 v196, v[244:245] offset:16384
	global_load_dwordx4 v[64:67], v189, s[2:3]
	v_mfma_f32_16x16x32_bf16 v[128:131], v[164:167], v[218:221], v[128:131]
	v_mfma_f32_16x16x32_bf16 v[124:127], v[172:175], v[218:221], v[124:127]
	s_waitcnt vmcnt(9)
	v_cvt_pk_bf16_f32 v244, v60, v61
	v_cvt_pk_bf16_f32 v245, v62, v63
	ds_write_b64 v197, v[244:245] offset:16384
	global_load_dwordx4 v[60:63], v189, s[48:49]
	v_mfma_f32_16x16x32_bf16 v[112:115], v[164:167], v[228:231], v[112:115]
	v_mfma_f32_16x16x32_bf16 v[108:111], v[172:175], v[228:231], v[108:111]
	s_waitcnt vmcnt(9)
	v_cvt_pk_bf16_f32 v244, v76, v77
	v_cvt_pk_bf16_f32 v245, v78, v79
	ds_write_b64 v195, v[244:245] offset:16384
	s_add_u32 s98, s2, 0x4000
	s_addc_u32 s99, s3, 0
	global_load_dwordx4 v[76:79], v189, s[98:99]
	v_mfma_f32_16x16x32_bf16 v[104:107], v[164:167], v[236:239], v[104:107]
	v_mfma_f32_16x16x32_bf16 v[100:103], v[172:175], v[236:239], v[100:103]
	s_waitcnt vmcnt(9)
	v_cvt_pk_bf16_f32 v244, v72, v73
	v_cvt_pk_bf16_f32 v245, v74, v75
	ds_write_b64 v197, v[244:245]
	s_add_u32 s100, s48, 0x4000
	s_addc_u32 s101, s49, 0
	global_load_dwordx4 v[72:75], v189, s[100:101]
	s_waitcnt lgkmcnt(4)
	v_mfma_f32_16x16x32_bf16 v[144:147], v[168:171], v[214:217], v[144:147]
	v_mfma_f32_16x16x32_bf16 v[140:143], v[176:179], v[214:217], v[140:143]
	s_waitcnt vmcnt(9)
	v_cvt_pk_bf16_f32 v244, v88, v89
	v_cvt_pk_bf16_f32 v245, v90, v91
	ds_write_b64 v194, v[244:245] offset:16384
	s_add_u32 s98, s2, 0x8000
	s_addc_u32 s99, s3, 0
	global_load_dwordx4 v[88:91], v189, s[98:99]
	v_mfma_f32_16x16x32_bf16 v[128:131], v[168:171], v[224:227], v[128:131]
	v_mfma_f32_16x16x32_bf16 v[124:127], v[176:179], v[224:227], v[124:127]
	s_waitcnt vmcnt(9)
	v_cvt_pk_bf16_f32 v244, v84, v85
	v_cvt_pk_bf16_f32 v245, v86, v87
	ds_write_b64 v196, v[244:245]
	s_add_u32 s100, s48, 0x8000
	s_addc_u32 s101, s49, 0
	global_load_dwordx4 v[84:87], v189, s[100:101]
	v_mfma_f32_16x16x32_bf16 v[112:115], v[168:171], v[232:235], v[112:115]
	v_mfma_f32_16x16x32_bf16 v[108:111], v[176:179], v[232:235], v[108:111]
	s_waitcnt vmcnt(9)
	v_cvt_pk_bf16_f32 v244, v96, v97
	v_cvt_pk_bf16_f32 v245, v98, v99
	ds_write_b64 v194, v[244:245]
	s_add_u32 s98, s2, 0xc000
	s_addc_u32 s99, s3, 0
	global_load_dwordx4 v[96:99], v189, s[98:99]
	v_mfma_f32_16x16x32_bf16 v[104:107], v[168:171], v[240:243], v[104:107]
	v_mfma_f32_16x16x32_bf16 v[100:103], v[176:179], v[240:243], v[100:103]
	s_waitcnt vmcnt(9)
	v_cvt_pk_bf16_f32 v244, v92, v93
	v_cvt_pk_bf16_f32 v245, v94, v95
	ds_write_b64 v195, v[244:245]
	s_add_u32 s100, s48, 0xc000
	s_addc_u32 s101, s49, 0
	global_load_dwordx4 v[92:95], v189, s[100:101]
	s_setprio 0
	s_branch .Lswp_dnO_tail
